# v45 + FFN-down residual epilogue: rows of H prefetched 4 iterations ahead into dead fragment registers with counted vmcnt waits (hipcc had 16 serialised load round trips per unit)
# speedup vs baseline: 1.0088x; 1.0007x over previous
; __device__ __forceinline__ unsigned cvt_pk_bf16(float lo, float hi) { unsigned r; asm volatile("v_cvt_pk_bf16_f32 %0, %1, %2" : "=v"(r) : "v"(lo), "v"(hi)); return r; }
;     __device__ __forceinline__ void operator()(const f32x4 (&acc)[2][2][4][2], const Unit& u, int wr, int wc, int fr, int fq) const {
;     ...
;         const float* base = x ? x + (size_t)(b * SEQ + (j - 1) * 256) * D : nullptr;
;         bf16_t* out = (bf16_t*)(ws + WS_H) + (size_t)u.pm * 256 * D;
;         const float* gate = (const float*)(ws + WS_MODF) + ((size_t)l * 3 + b) * ADAW + gate_idx * D + col0;
;         f32x4 gv[2][2];
; #pragma unroll
;         for (int bj = 0; bj < 2; ++bj)
; #pragma unroll
;             for (int n = 0; n < 2; ++n) gv[bj][n] = *(const f32x4*)(gate + bj * HALF + 4 * n);
; #pragma unroll
;         for (int ai = 0; ai < 2; ++ai)
; #pragma unroll
;             for (int m = 0; m < 4; ++m) { int r = wr * 64 + fr + ai * HALF + m * 16; asm volatile("" : "+v"(r)); const unsigned off = (unsigned)(r * D) + col0;
;                 f32x4 bs[2][2];
;                 if (base) {
; #pragma unroll
;                     for (int bj = 0; bj < 2; ++bj)
; #pragma unroll
;                         for (int n = 0; n < 2; ++n) bs[bj][n] = *(const f32x4*)(base + off + bj * HALF + 4 * n);
;                 } else {
; #pragma unroll
;                     for (int bj = 0; bj < 2; ++bj) { const u32x4 q = *(const u32x4*)(out + off + bj * HALF);
;                         bs[bj][0] = (f32x4){__uint_as_float(q.x << 16), __uint_as_float(q.x & 0xffff0000u), __uint_as_float(q.y << 16), __uint_as_float(q.y & 0xffff0000u)};
;                         bs[bj][1] = (f32x4){__uint_as_float(q.z << 16), __uint_as_float(q.z & 0xffff0000u), __uint_as_float(q.w << 16), __uint_as_float(q.w & 0xffff0000u)}; }
;                 }
; #pragma unroll
;                 for (int bj = 0; bj < 2; ++bj) { const f32x4 r0 = bs[bj][0] + gv[bj][0] * acc[ai][bj][m][0], r1 = bs[bj][1] + gv[bj][1] * acc[ai][bj][m][1];
;                     u32x4 w; w.x = cvt_pk_bf16(r0[0], r0[1]); w.y = cvt_pk_bf16(r0[2], r0[3]); w.z = cvt_pk_bf16(r1[0], r1[1]); w.w = cvt_pk_bf16(r1[2], r1[3]);
;                     *(u32x4*)(out + off + bj * HALF) = w; }
;                 asm volatile("" ::: "memory"); }
.LBB0_2528:
	s_mul_hi_i32 s2, s4, 0x78787879
	s_lshr_b32 s6, s2, 31
	s_ashr_i32 s2, s2, 3
	s_add_i32 s2, s2, s6
	s_mul_i32 s6, s2, 17
	s_sub_i32 s6, s4, s6
	v_lshl_or_b32 v160, s5, 8, v170
	s_cmp_lg_u32 s6, 0
	v_ashrrev_i32_e32 v161, 31, v160
	s_cbranch_scc0 .LBB0_2534
	s_ashr_i32 s5, s4, 31
	s_lshl_b64 s[4:5], s[4:5], 20
	s_mul_i32 s6, s2, 0xc000
	s_mul_hi_i32 s7, s2, 0xc000
	s_add_u32 s6, s0, s6
	s_addc_u32 s7, s1, s7
	v_lshl_add_u64 v[132:133], v[160:161], 2, s[6:7]
	s_mov_b64 s[6:7], 0x10a000
	v_lshl_add_u64 v[136:137], v[132:133], 0, s[6:7]
	s_mov_b32 s6, 0x10a000
	v_add_co_u32_e32 v132, vcc, s6, v132
	v_mov_b32_e32 v172, v131
	s_nop 0
	v_addc_co_u32_e32 v133, vcc, 0, v133, vcc
	global_load_dwordx4 v[144:147], v[132:133], off
	global_load_dwordx4 v[140:143], v[136:137], off offset:16
	s_nop 0
	global_load_dwordx4 v[132:135], v[136:137], off offset:528
	s_nop 0
	global_load_dwordx4 v[136:139], v[136:137], off offset:512
	s_add_u32 s4, s52, s4
	s_addc_u32 s5, s53, s5
	v_lshl_add_u32 v172, v172, 11, v160
	v_mov_b32_e32 v173, v130
	v_lshl_add_u64 v[176:177], v[172:173], 1, s[4:5]
	v_lshl_add_u32 v194, v131, 11, v160
	v_mov_b32_e32 v195, v130
	v_lshl_add_u64 v[194:195], v[194:195], 1, s[4:5]
	global_load_dwordx4 v[198:201], v[194:195], off
	global_load_dwordx4 v[202:205], v[194:195], off offset:256
	v_lshl_add_u32 v194, v163, 11, v160
	v_mov_b32_e32 v195, v130
	v_lshl_add_u64 v[194:195], v[194:195], 1, s[4:5]
	global_load_dwordx4 v[206:209], v[194:195], off
	global_load_dwordx4 v[210:213], v[194:195], off offset:256
	v_lshl_add_u32 v194, v164, 11, v160
	v_mov_b32_e32 v195, v130
	v_lshl_add_u64 v[194:195], v[194:195], 1, s[4:5]
	global_load_dwordx4 v[214:217], v[194:195], off
	global_load_dwordx4 v[218:221], v[194:195], off offset:256
	v_lshl_add_u32 v194, v165, 11, v160
	v_mov_b32_e32 v195, v130
	v_lshl_add_u64 v[194:195], v[194:195], 1, s[4:5]
	global_load_dwordx4 v[222:225], v[194:195], off
	global_load_dwordx4 v[226:229], v[194:195], off offset:256
	s_waitcnt vmcnt(6)
	v_lshlrev_b32_e32 v178, 16, v198
	v_and_b32_e32 v179, 0xffff0000, v198
	v_lshlrev_b32_e32 v180, 16, v199
	v_and_b32_e32 v181, 0xffff0000, v199
	v_lshlrev_b32_e32 v182, 16, v200
	v_and_b32_e32 v183, 0xffff0000, v200
	v_lshlrev_b32_e32 v184, 16, v201
	v_and_b32_e32 v185, 0xffff0000, v201
	v_lshlrev_b32_e32 v186, 16, v202
	v_and_b32_e32 v187, 0xffff0000, v202
	v_lshlrev_b32_e32 v188, 16, v203
	v_and_b32_e32 v189, 0xffff0000, v203
	v_pk_fma_f32 v[172:173], v[126:127], v[144:145], v[178:179]
	v_lshlrev_b32_e32 v190, 16, v204
	v_and_b32_e32 v191, 0xffff0000, v204
	v_lshlrev_b32_e32 v192, 16, v205
	v_and_b32_e32 v193, 0xffff0000, v205
	v_pk_fma_f32 v[174:175], v[128:129], v[146:147], v[180:181]
	v_cvt_pk_bf16_f32 v172, v172, v173
	v_pk_fma_f32 v[178:179], v[124:125], v[142:143], v[184:185]
	v_cvt_pk_bf16_f32 v173, v174, v175
	v_pk_fma_f32 v[180:181], v[122:123], v[140:141], v[182:183]
	s_nop 0
	v_cvt_pk_bf16_f32 v174, v180, v181
	v_cvt_pk_bf16_f32 v175, v178, v179
	global_store_dwordx4 v[176:177], v[172:175], off
	v_pk_fma_f32 v[178:179], v[112:113], v[134:135], v[192:193]
	v_pk_fma_f32 v[180:181], v[110:111], v[132:133], v[190:191]
	v_pk_fma_f32 v[172:173], v[118:119], v[136:137], v[186:187]
	v_pk_fma_f32 v[174:175], v[120:121], v[138:139], v[188:189]
	v_cvt_pk_bf16_f32 v172, v172, v173
	s_nop 0
	v_cvt_pk_bf16_f32 v173, v174, v175
	v_cvt_pk_bf16_f32 v174, v180, v181
	v_cvt_pk_bf16_f32 v175, v178, v179
	global_store_dwordx4 v[176:177], v[172:175], off offset:256
	s_nop 1
	v_lshl_add_u32 v194, v166, 11, v160
	v_mov_b32_e32 v195, v130
	v_lshl_add_u64 v[194:195], v[194:195], 1, s[4:5]
	global_load_dwordx4 v[198:201], v[194:195], off
	global_load_dwordx4 v[202:205], v[194:195], off offset:256
	v_mov_b32_e32 v172, v163
	v_mov_b32_e32 v173, v130
	v_lshl_add_u32 v172, v172, 11, v160
	v_lshl_add_u64 v[176:177], v[172:173], 1, s[4:5]
	s_waitcnt vmcnt(8)
	v_lshlrev_b32_e32 v178, 16, v206
	v_and_b32_e32 v179, 0xffff0000, v206
	v_lshlrev_b32_e32 v180, 16, v207
	v_and_b32_e32 v181, 0xffff0000, v207
	v_lshlrev_b32_e32 v182, 16, v208
	v_and_b32_e32 v183, 0xffff0000, v208
	v_lshlrev_b32_e32 v184, 16, v209
	v_and_b32_e32 v185, 0xffff0000, v209
	v_lshlrev_b32_e32 v186, 16, v210
	v_and_b32_e32 v187, 0xffff0000, v210
	v_lshlrev_b32_e32 v188, 16, v211
	v_and_b32_e32 v189, 0xffff0000, v211
	v_pk_fma_f32 v[172:173], v[114:115], v[144:145], v[178:179]
	v_lshlrev_b32_e32 v190, 16, v212
	v_and_b32_e32 v191, 0xffff0000, v212
	v_lshlrev_b32_e32 v192, 16, v213
	v_and_b32_e32 v193, 0xffff0000, v213
	v_pk_fma_f32 v[174:175], v[116:117], v[146:147], v[180:181]
	v_cvt_pk_bf16_f32 v172, v172, v173
	v_pk_fma_f32 v[178:179], v[108:109], v[142:143], v[184:185]
	v_cvt_pk_bf16_f32 v173, v174, v175
	v_pk_fma_f32 v[180:181], v[106:107], v[140:141], v[182:183]
	s_nop 0
	v_cvt_pk_bf16_f32 v174, v180, v181
	v_cvt_pk_bf16_f32 v175, v178, v179
	global_store_dwordx4 v[176:177], v[172:175], off
	v_pk_fma_f32 v[178:179], v[96:97], v[134:135], v[192:193]
	v_pk_fma_f32 v[180:181], v[94:95], v[132:133], v[190:191]
	v_pk_fma_f32 v[172:173], v[102:103], v[136:137], v[186:187]
	v_pk_fma_f32 v[174:175], v[104:105], v[138:139], v[188:189]
	v_cvt_pk_bf16_f32 v172, v172, v173
	s_nop 0
	v_cvt_pk_bf16_f32 v173, v174, v175
	v_cvt_pk_bf16_f32 v174, v180, v181
	v_cvt_pk_bf16_f32 v175, v178, v179
	global_store_dwordx4 v[176:177], v[172:175], off offset:256
	s_nop 1
	v_lshl_add_u32 v194, v167, 11, v160
	v_mov_b32_e32 v195, v130
	v_lshl_add_u64 v[194:195], v[194:195], 1, s[4:5]
	global_load_dwordx4 v[206:209], v[194:195], off
	global_load_dwordx4 v[210:213], v[194:195], off offset:256
	v_mov_b32_e32 v172, v164
	v_mov_b32_e32 v173, v130
	v_lshl_add_u32 v172, v172, 11, v160
	v_lshl_add_u64 v[176:177], v[172:173], 1, s[4:5]
	s_waitcnt vmcnt(10)
; __device__ __forceinline__ unsigned cvt_pk_bf16(float lo, float hi) { unsigned r; asm volatile("v_cvt_pk_bf16_f32 %0, %1, %2" : "=v"(r) : "v"(lo), "v"(hi)); return r; }
;     __device__ __forceinline__ void operator()(const f32x4 (&acc)[2][2][4][2], const Unit& u, int wr, int wc, int fr, int fq) const {
;     ...
;         const float* base = x ? x + (size_t)(b * SEQ + (j - 1) * 256) * D : nullptr;
;         bf16_t* out = (bf16_t*)(ws + WS_H) + (size_t)u.pm * 256 * D;
;         const float* gate = (const float*)(ws + WS_MODF) + ((size_t)l * 3 + b) * ADAW + gate_idx * D + col0;
;         f32x4 gv[2][2];
; #pragma unroll
;         for (int bj = 0; bj < 2; ++bj)
; #pragma unroll
;             for (int n = 0; n < 2; ++n) gv[bj][n] = *(const f32x4*)(gate + bj * HALF + 4 * n);
; #pragma unroll
;         for (int ai = 0; ai < 2; ++ai)
; #pragma unroll
;             for (int m = 0; m < 4; ++m) { int r = wr * 64 + fr + ai * HALF + m * 16; asm volatile("" : "+v"(r)); const unsigned off = (unsigned)(r * D) + col0;
;                 f32x4 bs[2][2];
;                 if (base) {
; #pragma unroll
;                     for (int bj = 0; bj < 2; ++bj)
; #pragma unroll
;                         for (int n = 0; n < 2; ++n) bs[bj][n] = *(const f32x4*)(base + off + bj * HALF + 4 * n);
;                 } else {
; #pragma unroll
;                     for (int bj = 0; bj < 2; ++bj) { const u32x4 q = *(const u32x4*)(out + off + bj * HALF);
;                         bs[bj][0] = (f32x4){__uint_as_float(q.x << 16), __uint_as_float(q.x & 0xffff0000u), __uint_as_float(q.y << 16), __uint_as_float(q.y & 0xffff0000u)};
;                         bs[bj][1] = (f32x4){__uint_as_float(q.z << 16), __uint_as_float(q.z & 0xffff0000u), __uint_as_float(q.w << 16), __uint_as_float(q.w & 0xffff0000u)}; }
;                 }
; #pragma unroll
;                 for (int bj = 0; bj < 2; ++bj) { const f32x4 r0 = bs[bj][0] + gv[bj][0] * acc[ai][bj][m][0], r1 = bs[bj][1] + gv[bj][1] * acc[ai][bj][m][1];
;                     u32x4 w; w.x = cvt_pk_bf16(r0[0], r0[1]); w.y = cvt_pk_bf16(r0[2], r0[3]); w.z = cvt_pk_bf16(r1[0], r1[1]); w.w = cvt_pk_bf16(r1[2], r1[3]);
;                     *(u32x4*)(out + off + bj * HALF) = w; }
;                 asm volatile("" ::: "memory"); }
	v_lshlrev_b32_e32 v178, 16, v214
	v_and_b32_e32 v179, 0xffff0000, v214
	v_lshlrev_b32_e32 v180, 16, v215
	v_and_b32_e32 v181, 0xffff0000, v215
	v_lshlrev_b32_e32 v182, 16, v216
	v_and_b32_e32 v183, 0xffff0000, v216
	v_lshlrev_b32_e32 v184, 16, v217
	v_and_b32_e32 v185, 0xffff0000, v217
	v_lshlrev_b32_e32 v186, 16, v218
	v_and_b32_e32 v187, 0xffff0000, v218
	v_lshlrev_b32_e32 v188, 16, v219
	v_and_b32_e32 v189, 0xffff0000, v219
	v_pk_fma_f32 v[172:173], v[98:99], v[144:145], v[178:179]
	v_lshlrev_b32_e32 v190, 16, v220
	v_and_b32_e32 v191, 0xffff0000, v220
	v_lshlrev_b32_e32 v192, 16, v221
	v_and_b32_e32 v193, 0xffff0000, v221
	v_pk_fma_f32 v[174:175], v[100:101], v[146:147], v[180:181]
	v_cvt_pk_bf16_f32 v172, v172, v173
	v_pk_fma_f32 v[178:179], v[92:93], v[142:143], v[184:185]
	v_cvt_pk_bf16_f32 v173, v174, v175
	v_pk_fma_f32 v[180:181], v[90:91], v[140:141], v[182:183]
	s_nop 0
	v_cvt_pk_bf16_f32 v174, v180, v181
	v_cvt_pk_bf16_f32 v175, v178, v179
	global_store_dwordx4 v[176:177], v[172:175], off
	v_pk_fma_f32 v[178:179], v[80:81], v[134:135], v[192:193]
	v_pk_fma_f32 v[180:181], v[78:79], v[132:133], v[190:191]
	v_pk_fma_f32 v[172:173], v[86:87], v[136:137], v[186:187]
	v_pk_fma_f32 v[174:175], v[88:89], v[138:139], v[188:189]
	v_cvt_pk_bf16_f32 v172, v172, v173
	s_nop 0
	v_cvt_pk_bf16_f32 v173, v174, v175
	v_cvt_pk_bf16_f32 v174, v180, v181
	v_cvt_pk_bf16_f32 v175, v178, v179
	global_store_dwordx4 v[176:177], v[172:175], off offset:256
	s_nop 1
	v_lshl_add_u32 v194, v168, 11, v160
	v_mov_b32_e32 v195, v130
	v_lshl_add_u64 v[194:195], v[194:195], 1, s[4:5]
	global_load_dwordx4 v[214:217], v[194:195], off
	global_load_dwordx4 v[218:221], v[194:195], off offset:256
	v_mov_b32_e32 v172, v165
	v_mov_b32_e32 v173, v130
	v_lshl_add_u32 v172, v172, 11, v160
	v_lshl_add_u64 v[176:177], v[172:173], 1, s[4:5]
	s_waitcnt vmcnt(12)
	v_lshlrev_b32_e32 v178, 16, v222
	v_and_b32_e32 v179, 0xffff0000, v222
	v_lshlrev_b32_e32 v180, 16, v223
	v_and_b32_e32 v181, 0xffff0000, v223
	v_lshlrev_b32_e32 v182, 16, v224
	v_and_b32_e32 v183, 0xffff0000, v224
	v_lshlrev_b32_e32 v184, 16, v225
	v_and_b32_e32 v185, 0xffff0000, v225
	v_lshlrev_b32_e32 v186, 16, v226
	v_and_b32_e32 v187, 0xffff0000, v226
	v_lshlrev_b32_e32 v188, 16, v227
	v_and_b32_e32 v189, 0xffff0000, v227
	v_pk_fma_f32 v[172:173], v[82:83], v[144:145], v[178:179]
	v_lshlrev_b32_e32 v190, 16, v228
	v_and_b32_e32 v191, 0xffff0000, v228
	v_lshlrev_b32_e32 v192, 16, v229
	v_and_b32_e32 v193, 0xffff0000, v229
	v_pk_fma_f32 v[174:175], v[84:85], v[146:147], v[180:181]
	v_cvt_pk_bf16_f32 v172, v172, v173
	v_pk_fma_f32 v[178:179], v[76:77], v[142:143], v[184:185]
	v_cvt_pk_bf16_f32 v173, v174, v175
	v_pk_fma_f32 v[180:181], v[74:75], v[140:141], v[182:183]
	s_nop 0
	v_cvt_pk_bf16_f32 v174, v180, v181
	v_cvt_pk_bf16_f32 v175, v178, v179
	global_store_dwordx4 v[176:177], v[172:175], off
	v_pk_fma_f32 v[178:179], v[68:69], v[134:135], v[192:193]
	v_pk_fma_f32 v[180:181], v[66:67], v[132:133], v[190:191]
	v_pk_fma_f32 v[172:173], v[70:71], v[136:137], v[186:187]
	v_pk_fma_f32 v[174:175], v[72:73], v[138:139], v[188:189]
	v_cvt_pk_bf16_f32 v172, v172, v173
	s_nop 0
	v_cvt_pk_bf16_f32 v173, v174, v175
	v_cvt_pk_bf16_f32 v174, v180, v181
	v_cvt_pk_bf16_f32 v175, v178, v179
	global_store_dwordx4 v[176:177], v[172:175], off offset:256
	s_nop 1
	v_lshl_add_u32 v194, v169, 11, v160
	v_mov_b32_e32 v195, v130
	v_lshl_add_u64 v[194:195], v[194:195], 1, s[4:5]
	global_load_dwordx4 v[222:225], v[194:195], off
	global_load_dwordx4 v[226:229], v[194:195], off offset:256
	v_mov_b32_e32 v172, v166
	v_mov_b32_e32 v173, v130
	v_lshl_add_u32 v172, v172, 11, v160
	v_lshl_add_u64 v[176:177], v[172:173], 1, s[4:5]
	s_waitcnt vmcnt(12)
	v_lshlrev_b32_e32 v178, 16, v198
	v_and_b32_e32 v179, 0xffff0000, v198
	v_lshlrev_b32_e32 v180, 16, v199
	v_and_b32_e32 v181, 0xffff0000, v199
	v_lshlrev_b32_e32 v182, 16, v200
	v_and_b32_e32 v183, 0xffff0000, v200
	v_lshlrev_b32_e32 v184, 16, v201
	v_and_b32_e32 v185, 0xffff0000, v201
	v_lshlrev_b32_e32 v186, 16, v202
	v_and_b32_e32 v187, 0xffff0000, v202
	v_lshlrev_b32_e32 v188, 16, v203
	v_and_b32_e32 v189, 0xffff0000, v203
	v_pk_fma_f32 v[172:173], v[62:63], v[144:145], v[178:179]
	v_lshlrev_b32_e32 v190, 16, v204
	v_and_b32_e32 v191, 0xffff0000, v204
	v_lshlrev_b32_e32 v192, 16, v205
	v_and_b32_e32 v193, 0xffff0000, v205
	v_pk_fma_f32 v[174:175], v[64:65], v[146:147], v[180:181]
	v_cvt_pk_bf16_f32 v172, v172, v173
	v_pk_fma_f32 v[178:179], v[60:61], v[142:143], v[184:185]
	v_cvt_pk_bf16_f32 v173, v174, v175
	v_pk_fma_f32 v[180:181], v[58:59], v[140:141], v[182:183]
	s_nop 0
	v_cvt_pk_bf16_f32 v174, v180, v181
	v_cvt_pk_bf16_f32 v175, v178, v179
	global_store_dwordx4 v[176:177], v[172:175], off
	v_pk_fma_f32 v[178:179], v[48:49], v[134:135], v[192:193]
	v_pk_fma_f32 v[180:181], v[46:47], v[132:133], v[190:191]
	v_pk_fma_f32 v[172:173], v[54:55], v[136:137], v[186:187]
	v_pk_fma_f32 v[174:175], v[56:57], v[138:139], v[188:189]
	v_cvt_pk_bf16_f32 v172, v172, v173
	s_nop 0
	v_cvt_pk_bf16_f32 v173, v174, v175
	v_cvt_pk_bf16_f32 v174, v180, v181
	v_cvt_pk_bf16_f32 v175, v178, v179
	global_store_dwordx4 v[176:177], v[172:175], off offset:256
	s_nop 1
	v_mov_b32_e32 v172, v167
	v_mov_b32_e32 v173, v130
	v_lshl_add_u32 v172, v172, 11, v160
	v_lshl_add_u64 v[176:177], v[172:173], 1, s[4:5]
	s_waitcnt vmcnt(10)
; __device__ __forceinline__ unsigned cvt_pk_bf16(float lo, float hi) { unsigned r; asm volatile("v_cvt_pk_bf16_f32 %0, %1, %2" : "=v"(r) : "v"(lo), "v"(hi)); return r; }
;     __device__ __forceinline__ void operator()(const f32x4 (&acc)[2][2][4][2], const Unit& u, int wr, int wc, int fr, int fq) const {
;     ...
;         const float* base = x ? x + (size_t)(b * SEQ + (j - 1) * 256) * D : nullptr;
;         bf16_t* out = (bf16_t*)(ws + WS_H) + (size_t)u.pm * 256 * D;
;         const float* gate = (const float*)(ws + WS_MODF) + ((size_t)l * 3 + b) * ADAW + gate_idx * D + col0;
;         f32x4 gv[2][2];
; #pragma unroll
;         for (int bj = 0; bj < 2; ++bj)
; #pragma unroll
;             for (int n = 0; n < 2; ++n) gv[bj][n] = *(const f32x4*)(gate + bj * HALF + 4 * n);
; #pragma unroll
;         for (int ai = 0; ai < 2; ++ai)
; #pragma unroll
;             for (int m = 0; m < 4; ++m) { int r = wr * 64 + fr + ai * HALF + m * 16; asm volatile("" : "+v"(r)); const unsigned off = (unsigned)(r * D) + col0;
;                 f32x4 bs[2][2];
;                 if (base) {
; #pragma unroll
;                     for (int bj = 0; bj < 2; ++bj)
; #pragma unroll
;                         for (int n = 0; n < 2; ++n) bs[bj][n] = *(const f32x4*)(base + off + bj * HALF + 4 * n);
;                 } else {
; #pragma unroll
;                     for (int bj = 0; bj < 2; ++bj) { const u32x4 q = *(const u32x4*)(out + off + bj * HALF);
;                         bs[bj][0] = (f32x4){__uint_as_float(q.x << 16), __uint_as_float(q.x & 0xffff0000u), __uint_as_float(q.y << 16), __uint_as_float(q.y & 0xffff0000u)};
;                         bs[bj][1] = (f32x4){__uint_as_float(q.z << 16), __uint_as_float(q.z & 0xffff0000u), __uint_as_float(q.w << 16), __uint_as_float(q.w & 0xffff0000u)}; }
;                 }
; #pragma unroll
;                 for (int bj = 0; bj < 2; ++bj) { const f32x4 r0 = bs[bj][0] + gv[bj][0] * acc[ai][bj][m][0], r1 = bs[bj][1] + gv[bj][1] * acc[ai][bj][m][1];
;                     u32x4 w; w.x = cvt_pk_bf16(r0[0], r0[1]); w.y = cvt_pk_bf16(r0[2], r0[3]); w.z = cvt_pk_bf16(r1[0], r1[1]); w.w = cvt_pk_bf16(r1[2], r1[3]);
;                     *(u32x4*)(out + off + bj * HALF) = w; }
;                 asm volatile("" ::: "memory"); }
	v_lshlrev_b32_e32 v178, 16, v206
	v_and_b32_e32 v179, 0xffff0000, v206
	v_lshlrev_b32_e32 v180, 16, v207
	v_and_b32_e32 v181, 0xffff0000, v207
	v_lshlrev_b32_e32 v182, 16, v208
	v_and_b32_e32 v183, 0xffff0000, v208
	v_lshlrev_b32_e32 v184, 16, v209
	v_and_b32_e32 v185, 0xffff0000, v209
	v_lshlrev_b32_e32 v186, 16, v210
	v_and_b32_e32 v187, 0xffff0000, v210
	v_lshlrev_b32_e32 v188, 16, v211
	v_and_b32_e32 v189, 0xffff0000, v211
	v_pk_fma_f32 v[172:173], v[50:51], v[144:145], v[178:179]
	v_lshlrev_b32_e32 v190, 16, v212
	v_and_b32_e32 v191, 0xffff0000, v212
	v_lshlrev_b32_e32 v192, 16, v213
	v_and_b32_e32 v193, 0xffff0000, v213
	v_pk_fma_f32 v[174:175], v[52:53], v[146:147], v[180:181]
	v_cvt_pk_bf16_f32 v172, v172, v173
	v_pk_fma_f32 v[178:179], v[44:45], v[142:143], v[184:185]
	v_cvt_pk_bf16_f32 v173, v174, v175
	v_pk_fma_f32 v[180:181], v[42:43], v[140:141], v[182:183]
	s_nop 0
	v_cvt_pk_bf16_f32 v174, v180, v181
	v_cvt_pk_bf16_f32 v175, v178, v179
	global_store_dwordx4 v[176:177], v[172:175], off
	v_pk_fma_f32 v[178:179], v[32:33], v[134:135], v[192:193]
	v_pk_fma_f32 v[180:181], v[30:31], v[132:133], v[190:191]
	v_pk_fma_f32 v[172:173], v[38:39], v[136:137], v[186:187]
	v_pk_fma_f32 v[174:175], v[40:41], v[138:139], v[188:189]
	v_cvt_pk_bf16_f32 v172, v172, v173
	s_nop 0
	v_cvt_pk_bf16_f32 v173, v174, v175
	v_cvt_pk_bf16_f32 v174, v180, v181
	v_cvt_pk_bf16_f32 v175, v178, v179
	global_store_dwordx4 v[176:177], v[172:175], off offset:256
	s_nop 1
	v_mov_b32_e32 v172, v168
	v_mov_b32_e32 v173, v130
	v_lshl_add_u32 v172, v172, 11, v160
	v_lshl_add_u64 v[176:177], v[172:173], 1, s[4:5]
	s_waitcnt vmcnt(8)
	v_lshlrev_b32_e32 v178, 16, v214
	v_and_b32_e32 v179, 0xffff0000, v214
	v_lshlrev_b32_e32 v180, 16, v215
	v_and_b32_e32 v181, 0xffff0000, v215
	v_lshlrev_b32_e32 v182, 16, v216
	v_and_b32_e32 v183, 0xffff0000, v216
	v_lshlrev_b32_e32 v184, 16, v217
	v_and_b32_e32 v185, 0xffff0000, v217
	v_lshlrev_b32_e32 v186, 16, v218
	v_and_b32_e32 v187, 0xffff0000, v218
	v_lshlrev_b32_e32 v188, 16, v219
	v_and_b32_e32 v189, 0xffff0000, v219
	v_pk_fma_f32 v[172:173], v[34:35], v[144:145], v[178:179]
	v_lshlrev_b32_e32 v190, 16, v220
	v_and_b32_e32 v191, 0xffff0000, v220
	v_lshlrev_b32_e32 v192, 16, v221
	v_and_b32_e32 v193, 0xffff0000, v221
	v_pk_fma_f32 v[174:175], v[36:37], v[146:147], v[180:181]
	v_cvt_pk_bf16_f32 v172, v172, v173
	v_pk_fma_f32 v[178:179], v[28:29], v[142:143], v[184:185]
	v_cvt_pk_bf16_f32 v173, v174, v175
	v_pk_fma_f32 v[180:181], v[26:27], v[140:141], v[182:183]
	s_nop 0
	v_cvt_pk_bf16_f32 v174, v180, v181
	v_cvt_pk_bf16_f32 v175, v178, v179
	global_store_dwordx4 v[176:177], v[172:175], off
	v_pk_fma_f32 v[178:179], v[16:17], v[134:135], v[192:193]
	v_pk_fma_f32 v[180:181], v[14:15], v[132:133], v[190:191]
	v_pk_fma_f32 v[172:173], v[22:23], v[136:137], v[186:187]
	v_pk_fma_f32 v[174:175], v[24:25], v[138:139], v[188:189]
	v_cvt_pk_bf16_f32 v172, v172, v173
	s_nop 0
	v_cvt_pk_bf16_f32 v173, v174, v175
	v_cvt_pk_bf16_f32 v174, v180, v181
	v_cvt_pk_bf16_f32 v175, v178, v179
	global_store_dwordx4 v[176:177], v[172:175], off offset:256
	s_nop 1
	v_mov_b32_e32 v172, v169
	v_mov_b32_e32 v173, v130
	v_lshl_add_u32 v172, v172, 11, v160
	v_lshl_add_u64 v[176:177], v[172:173], 1, s[4:5]
	s_waitcnt vmcnt(6)
	v_lshlrev_b32_e32 v178, 16, v222
	v_and_b32_e32 v179, 0xffff0000, v222
	v_lshlrev_b32_e32 v180, 16, v223
	v_and_b32_e32 v181, 0xffff0000, v223
	v_lshlrev_b32_e32 v182, 16, v224
	v_and_b32_e32 v183, 0xffff0000, v224
	v_lshlrev_b32_e32 v184, 16, v225
	v_and_b32_e32 v185, 0xffff0000, v225
	v_pk_fma_f32 v[146:147], v[20:21], v[146:147], v[180:181]
	v_pk_fma_f32 v[144:145], v[18:19], v[144:145], v[178:179]
	v_pk_fma_f32 v[178:179], v[12:13], v[142:143], v[184:185]
	v_pk_fma_f32 v[142:143], v[10:11], v[140:141], v[182:183]
	v_cvt_pk_bf16_f32 v140, v144, v145
	v_cvt_pk_bf16_f32 v141, v146, v147
	v_lshlrev_b32_e32 v188, 16, v228
	v_and_b32_e32 v189, 0xffff0000, v228
	v_lshlrev_b32_e32 v174, 16, v229
	v_and_b32_e32 v175, 0xffff0000, v229
	v_lshlrev_b32_e32 v186, 16, v226
	v_and_b32_e32 v187, 0xffff0000, v226
	v_lshlrev_b32_e32 v172, 16, v227
	v_and_b32_e32 v173, 0xffff0000, v227
	v_cvt_pk_bf16_f32 v142, v142, v143
	v_cvt_pk_bf16_f32 v143, v178, v179
	global_store_dwordx4 v[176:177], v[140:143], off
	v_pk_fma_f32 v[138:139], v[8:9], v[138:139], v[172:173]
	v_pk_fma_f32 v[136:137], v[6:7], v[136:137], v[186:187]
	v_pk_fma_f32 v[140:141], v[4:5], v[134:135], v[174:175]
	v_pk_fma_f32 v[134:135], v[2:3], v[132:133], v[188:189]
	v_cvt_pk_bf16_f32 v132, v136, v137
	v_cvt_pk_bf16_f32 v133, v138, v139
	s_nop 0
	v_cvt_pk_bf16_f32 v134, v134, v135
	v_cvt_pk_bf16_f32 v135, v140, v141
	global_store_dwordx4 v[176:177], v[132:135], off offset:256
	s_cbranch_execnz .LBB0_2531
